# MoE scheduler next(): 31-compare LDS chain replaced by lane-parallel compare + popcount (P7,P8)
# speedup vs baseline: 1.0127x; 1.0127x over previous
; __device__ __forceinline__ bool tile_order(long L, int nM, int nN, int& pm, int& pn) {
;     const int nwg = nM * nN; if (L >= nwg) return false;
;     int wgid = (int)L; { const int q = nwg / 8, r = nwg % 8, xcd = wgid % 8, off = wgid / 8; wgid = (xcd < r ? xcd * (q + 1) : r * (q + 1) + (xcd - r) * q) + off; }
;     const int nig = WGM * nN, gid = wgid / nig, fm = gid * WGM, gsz = (nM - fm) < WGM ? (nM - fm) : WGM;
;     pm = fm + ((wgid % nig) % gsz); pn = (wgid % nig) / gsz; return true;
;     __device__ __forceinline__ bool next(int i, Unit& u) const {
;         const int nM = __builtin_amdgcn_readfirstlane(tstart[NE]); int pm, pn; if (!tile_order((long)i * G + c, nM, nN, pm, pn)) return false;
;         int e = 0;
;         for (int j = 1; j < NE; ++j) e += (tstart[j] <= pm) ? 1 : 0;
;         e = __builtin_amdgcn_readfirstlane(e);
;         const int mt = __builtin_amdgcn_readfirstlane(pm - tstart[e]);
;         u.pm = pm; u.pn = pn; u.e = e;
;         u.avalid = __builtin_amdgcn_readfirstlane(cnt[e]) - mt * 256;
;         u.aidx = stok + (size_t)e * T + mt * 256;
;         u.aBase = GATHER ? A : A + (size_t)(GATHER_ ? (pm & 127) : pm) * 256 * ROWB;
;         u.bBase = Bt + ((size_t)e * nrowsB + (size_t)pn * 256) * ROWB;
.LBB0_727:
	v_mbcnt_lo_u32_b32 v7, -1, 0
	v_mbcnt_hi_u32_b32 v7, -1, v7
	v_lshlrev_b32_e32 v7, 2, v7
	v_add_u32_e32 v5, 0x27d00, v7
	v_add_u32_e32 v6, 0x27e00, v7
	ds_read_b32 v5, v5
	ds_read_b32 v6, v6
	s_add_i32 s95, s95, 1
	s_mul_i32 s2, s95, s96
	s_mul_hi_u32 s3, s95, s33
	s_add_i32 s3, s3, s2
	s_mul_i32 s2, s95, s33
	s_waitcnt lgkmcnt(0)
	v_readlane_b32 s18, v5, 32
	s_add_u32 s30, s2, s77
	s_addc_u32 s31, s3, s51
	s_lshl_b32 s2, s18, 4
	s_ashr_i32 s3, s2, 31
	v_mov_b64_e32 v[2:3], s[2:3]
	v_cmp_ge_i64_e32 vcc, s[30:31], v[2:3]
	v_cmp_lt_i64_e64 s[2:3], s[30:31], v[2:3]
	s_cbranch_vccnz .LBB0_729
	s_ashr_i32 s20, s30, 31
	s_lshr_b32 s20, s20, 29
	s_add_i32 s20, s30, s20
	s_ashr_i32 s21, s20, 3
	s_and_b32 s20, s20, -8
	s_sub_i32 s20, s30, s20
	v_mov_b32_e32 v2, s20
	v_alignbit_b32 v2, s18, v2, 31
	s_nop 0
	v_readfirstlane_b32 s22, v2
	s_mul_i32 s20, s20, s22
	s_add_i32 s20, s20, s21
	s_ashr_i32 s21, s20, 31
	s_lshr_b32 s21, s21, 26
	s_add_i32 s21, s20, s21
	s_ashr_i32 s22, s21, 6
	s_lshl_b32 s22, s22, 2
	s_sub_i32 s18, s18, s22
	s_min_i32 s18, s18, 4
	s_abs_i32 s23, s18
	v_cvt_f32_u32_e32 v2, s23
	s_sub_i32 s25, 0, s23
	s_andn2_b32 s21, s21, 63
	s_sub_i32 s20, s20, s21
	v_rcp_iflag_f32_e32 v2, v2
	s_abs_i32 s21, s20
	s_xor_b32 s24, s20, s18
	s_ashr_i32 s24, s24, 31
	v_mul_f32_e32 v2, 0x4f7ffffe, v2
	v_cvt_u32_f32_e32 v2, v2
	s_nop 0
	v_readfirstlane_b32 s27, v2
	s_mul_i32 s25, s25, s27
	s_mul_hi_u32 s25, s27, s25
	s_add_i32 s27, s27, s25
	s_mul_hi_u32 s25, s21, s27
	s_mul_i32 s27, s25, s23
	s_sub_i32 s21, s21, s27
	s_add_i32 s30, s25, 1
	s_sub_i32 s27, s21, s23
	s_cmp_ge_u32 s21, s23
	s_cselect_b32 s25, s30, s25
	s_cselect_b32 s21, s27, s21
	s_add_i32 s27, s25, 1
	s_cmp_ge_u32 s21, s23
	s_cselect_b32 s21, s27, s25
	s_xor_b32 s21, s21, s24
	s_sub_i32 s44, s21, s24
	s_mul_i32 s18, s44, s18
	s_sub_i32 s18, s20, s18
	s_add_i32 s97, s22, s18
	v_cmp_ge_i32_e32 vcc, s97, v5
	s_nop 3
	s_and_b32 vcc_lo, vcc_lo, 0xfffffffe
	s_bcnt1_i32_b32 s20, vcc_lo
	s_nop 3
	v_readlane_b32 s18, v5, s20
	v_readlane_b32 s23, v6, s20
	s_ashr_i32 s21, s20, 31
	s_lshl_b64 s[24:25], s[20:21], 17
	s_sub_i32 s18, s97, s18
	s_lshl_b32 s22, s18, 8
	s_sub_i32 s90, s23, s22
	v_readlane_b32 s18, v255, 6
	s_add_u32 s18, s18, s24
	v_readlane_b32 s23, v255, 22
	s_addc_u32 s24, s23, s25
	s_ashr_i32 s23, s22, 31
	s_lshl_b64 s[22:23], s[22:23], 2
	s_add_u32 s22, s18, s22
	s_addc_u32 s23, s24, s23
	s_ashr_i32 s45, s44, 31
	s_lshl_b64 s[24:25], s[44:45], 19
	s_lshl_b64 s[30:31], s[20:21], 23
	v_readlane_b32 s18, v255, 51
	s_add_u32 s18, s18, s24
	v_readlane_b32 s21, v255, 52
	s_addc_u32 s21, s21, s25
	s_add_u32 s24, s18, s30
	s_addc_u32 s25, s21, s31

; #define PG8_STAGE(bufoff, gbase, voff) do { if constexpr (!(Sched::CRIP & 2)) _Pragma("unroll") for (int _i = 0; _i < 2; ++_i) { unsigned _o = (voff)[_i]; asm volatile("" : "+v"(_o)); \
;         __builtin_amdgcn_global_load_lds((const unsigned*)((const char*)(gbase) + _o), (LAS unsigned*)(lds + (bufoff) + ldsw + _i * 8192), 16, 0, 0); } } while (0)
; #define PG8_LDA(dst, b, h) do { if constexpr (!(Sched::CRIP & 4)) _Pragma("unroll") for (int m = 0; m < 4; ++m) dst[m] = PG8_CAT(*(const LAS i32x4*)(lds + PG8_SA(b, h) + aoff + m * 2048), *(const LAS i32x4*)(lds + PG8_SA(b, h) + aoff + m * 2048 + 1024)); } while (0)
; #define PG8_LDB(dst, b, h) do { if constexpr (!(Sched::CRIP & 4)) _Pragma("unroll") for (int n = 0; n < 2; ++n) dst[n] = PG8_CAT(*(const LAS i32x4*)(lds + PG8_SB(b, h) + boff + n * 2048), *(const LAS i32x4*)(lds + PG8_SB(b, h) + boff + n * 2048 + 1024)); } while (0)
; #define PG8_WAIT_V(n) asm volatile("s_waitcnt vmcnt(" #n ")" ::: "memory")
; #define PG8_WAIT_L(n) asm volatile("s_waitcnt lgkmcnt(" #n ")" ::: "memory")
; #define PG8_BAR __builtin_amdgcn_s_barrier()
; #define PG8_SCHED __builtin_amdgcn_sched_barrier(0)
; template <class Epi, class Sched>
; __device__ __forceinline__ void gemm_phase(LAS unsigned char* lds, const Sched& S, const Epi& E) {
;     ...
;             PG8_LDA(At, 0, 1); PG8_STAGE(PG8_SB(0, 0), b2, voffB); PG8_STAGE(PG8_SB(0, 1), b2 + hstep, voffB); PG8_STAGE(PG8_SA(0, 0), a2, vA[0]);
;             PG8_WAIT_V(8); PG8_WAIT_L(0); PG8_BAR; PG8_MMA(1, 0, At, B0); PG8_MMA(1, 1, At, B1); PG8_BAR2; PG8_SCHED;
;             PG8_LDB(B0, 1, 0); PG8_LDB(B1, 1, 1); PG8_SCHED; PG8_LDA(At, 1, 0); PG8_STAGE(PG8_SA(0, 1), a2, vA[1]);
;             PG8_WAIT_V(8); PG8_WAIT_L(0); PG8_BAR; PG8_MMA(0, 0, At, B0); PG8_MMA(0, 1, At, B1); PG8_BAR2; PG8_SCHED;
.LBB0_734:
	s_add_i32 s30, s21, 0x80
	s_and_b32 s53, s30, 0x780
	s_and_b64 s[30:31], s[34:35], exec
	s_cselect_b32 s31, s19, s53
	s_cselect_b32 s30, 0, 0
	s_add_u32 s36, s58, s31
	s_addc_u32 s37, s59, s30
	s_add_u32 s53, s28, s53
	s_addc_u32 s54, s29, 0
	s_and_b64 s[30:31], s[34:35], exec
	s_cselect_b32 s55, s46, s54
	s_cselect_b32 s54, s45, s53
	s_addk_i32 s21, 0x100
	s_and_b32 s53, s21, 0x780
	s_and_b64 s[30:31], s[34:35], exec
	s_cselect_b32 s30, s47, s53
	s_cselect_b32 s31, 0, 0
	s_add_u32 s30, s58, s30
	s_addc_u32 s31, s59, s31
	v_mov_b32_e32 v45, v1
	s_mov_b32 m0, s63
	s_add_u32 s53, s28, s53
	ds_read_b128 v[204:207], v200 offset:16384
	ds_read_b128 v[208:211], v200 offset:17408
	ds_read_b128 v[214:217], v200 offset:18432
	ds_read_b128 v[218:221], v200 offset:19456
	ds_read_b128 v[222:225], v200 offset:20480
	ds_read_b128 v[226:229], v200 offset:21504
	ds_read_b128 v[230:233], v200 offset:22528
	ds_read_b128 v[234:237], v200 offset:23552
	s_addc_u32 vcc_lo, s29, 0
	global_load_lds_dwordx4 v45, s[54:55]
	v_mov_b32_e32 v45, v190
	s_and_b64 s[34:35], s[34:35], exec
	s_mov_b32 m0, s64
	s_cselect_b32 s35, s49, vcc_lo
	s_cselect_b32 s34, s48, s53
	global_load_lds_dwordx4 v45, s[54:55]
	s_add_u32 s54, s54, 0x40000
	v_mov_b32_e32 v45, v1
	s_addc_u32 s55, s55, 0
	s_mov_b32 m0, s65
	s_nop 0
	global_load_lds_dwordx4 v45, s[54:55]
	v_mov_b32_e32 v45, v190
	s_mov_b32 m0, s66
	s_nop 0
	global_load_lds_dwordx4 v45, s[54:55]
	v_mov_b32_e32 v45, v192
	s_mov_b32 m0, s39
	s_nop 0
	global_load_lds_dwordx4 v45, s[36:37]
	v_mov_b32_e32 v45, v194
	s_mov_b32 m0, s67
	s_nop 0
	global_load_lds_dwordx4 v45, s[36:37]
	s_waitcnt vmcnt(8)
	s_waitcnt lgkmcnt(0)
	s_barrier
	s_setprio 1
	s_waitcnt lgkmcnt(0)
	s_nop 1
	v_mfma_scale_f32_16x16x128_f8f6f4 v[118:121], v[2:9], v[204:211], v[118:121], v191, v191 op_sel_hi:[0,0,0]
	v_mfma_scale_f32_16x16x128_f8f6f4 v[110:113], v[18:25], v[204:211], v[110:113], v191, v191 op_sel_hi:[0,0,0]
	v_mfma_scale_f32_16x16x128_f8f6f4 v[98:101], v[2:9], v[214:221], v[98:101], v191, v191 op_sel_hi:[0,0,0]
	v_mfma_scale_f32_16x16x128_f8f6f4 v[90:93], v[18:25], v[214:221], v[90:93], v191, v191 op_sel_hi:[0,0,0]
	v_mfma_scale_f32_16x16x128_f8f6f4 v[82:85], v[2:9], v[222:229], v[82:85], v191, v191 op_sel_hi:[0,0,0]
	v_mfma_scale_f32_16x16x128_f8f6f4 v[66:69], v[18:25], v[222:229], v[66:69], v191, v191 op_sel_hi:[0,0,0]
	v_mfma_scale_f32_16x16x128_f8f6f4 v[58:61], v[2:9], v[230:237], v[58:61], v191, v191 op_sel_hi:[0,0,0]
	v_mfma_scale_f32_16x16x128_f8f6f4 v[50:53], v[18:25], v[230:237], v[50:53], v191, v191 op_sel_hi:[0,0,0]
	s_setprio 0
	s_setprio 1
	s_nop 1
	v_mfma_scale_f32_16x16x128_f8f6f4 v[106:109], v[10:17], v[204:211], v[106:109], v191, v191 op_sel_hi:[0,0,0]
	v_mfma_scale_f32_16x16x128_f8f6f4 v[114:117], v[26:33], v[204:211], v[114:117], v191, v191 op_sel_hi:[0,0,0]
	v_mfma_scale_f32_16x16x128_f8f6f4 v[102:105], v[10:17], v[214:221], v[102:105], v191, v191 op_sel_hi:[0,0,0]
	v_mfma_scale_f32_16x16x128_f8f6f4 v[94:97], v[26:33], v[214:221], v[94:97], v191, v191 op_sel_hi:[0,0,0]
	v_mfma_scale_f32_16x16x128_f8f6f4 v[86:89], v[10:17], v[222:229], v[86:89], v191, v191 op_sel_hi:[0,0,0]
	v_mfma_scale_f32_16x16x128_f8f6f4 v[70:73], v[26:33], v[222:229], v[70:73], v191, v191 op_sel_hi:[0,0,0]
	v_mfma_scale_f32_16x16x128_f8f6f4 v[62:65], v[10:17], v[230:237], v[62:65], v191, v191 op_sel_hi:[0,0,0]
	v_mfma_scale_f32_16x16x128_f8f6f4 v[54:57], v[26:33], v[230:237], v[54:57], v191, v191 op_sel_hi:[0,0,0]
	s_setprio 0
	s_barrier
	ds_read_b128 v[2:5], v43
	ds_read_b128 v[6:9], v43 offset:1024
	ds_read_b128 v[10:13], v43 offset:2048
	ds_read_b128 v[14:17], v43 offset:3072
	ds_read_b128 v[18:21], v44
	ds_read_b128 v[22:25], v44 offset:1024
	ds_read_b128 v[26:29], v44 offset:2048
	ds_read_b128 v[30:33], v44 offset:3072
	v_mov_b32_e32 v45, v193
	s_mov_b32 m0, s68
	ds_read_b128 v[204:207], v200 offset:32768
	ds_read_b128 v[208:211], v200 offset:33792
	ds_read_b128 v[214:217], v200 offset:34816
	ds_read_b128 v[218:221], v200 offset:35840
	ds_read_b128 v[222:225], v200 offset:36864
	ds_read_b128 v[226:229], v200 offset:37888
	ds_read_b128 v[230:233], v200 offset:38912
	ds_read_b128 v[234:237], v200 offset:39936
	s_nop 0
	global_load_lds_dwordx4 v45, s[36:37]
	v_mov_b32_e32 v45, v195
	s_mov_b32 m0, s69
	s_nop 0
	global_load_lds_dwordx4 v45, s[36:37]
	s_waitcnt vmcnt(8)
	s_waitcnt lgkmcnt(0)
	s_barrier
; #define PG8_STAGE(bufoff, gbase, voff) do { if constexpr (!(Sched::CRIP & 2)) _Pragma("unroll") for (int _i = 0; _i < 2; ++_i) { unsigned _o = (voff)[_i]; asm volatile("" : "+v"(_o)); \
;         __builtin_amdgcn_global_load_lds((const unsigned*)((const char*)(gbase) + _o), (LAS unsigned*)(lds + (bufoff) + ldsw + _i * 8192), 16, 0, 0); } } while (0)
; #define PG8_LDA(dst, b, h) do { if constexpr (!(Sched::CRIP & 4)) _Pragma("unroll") for (int m = 0; m < 4; ++m) dst[m] = PG8_CAT(*(const LAS i32x4*)(lds + PG8_SA(b, h) + aoff + m * 2048), *(const LAS i32x4*)(lds + PG8_SA(b, h) + aoff + m * 2048 + 1024)); } while (0)
; #define PG8_WAIT_V(n) asm volatile("s_waitcnt vmcnt(" #n ")" ::: "memory")
; #define PG8_WAIT_L(n) asm volatile("s_waitcnt lgkmcnt(" #n ")" ::: "memory")
; #define PG8_BAR __builtin_amdgcn_s_barrier()
; #define PG8_SCHED __builtin_amdgcn_sched_barrier(0)
; template <class Epi, class Sched>
; __device__ __forceinline__ void gemm_phase(LAS unsigned char* lds, const Sched& S, const Epi& E) {
;     ...
;             PG8_WAIT_V(8); PG8_WAIT_L(0); PG8_BAR; PG8_MMA(0, 0, At, B0); PG8_MMA(0, 1, At, B1); PG8_BAR2; PG8_SCHED;
;             PG8_LDA(At, 1, 1); PG8_STAGE(PG8_SB(1, 0), b3, voffB); PG8_STAGE(PG8_SB(1, 1), b3 + hstep, voffB); PG8_STAGE(PG8_SA(1, 0), a3, vA[0]);
;             PG8_WAIT_V(8); PG8_WAIT_L(0); PG8_BAR; PG8_MMA(1, 0, At, B0); PG8_MMA(1, 1, At, B1); PG8_BAR2; PG8_SCHED;
	s_setprio 1
	s_waitcnt lgkmcnt(0)
	s_nop 1
	v_mfma_scale_f32_16x16x128_f8f6f4 v[178:181], v[2:9], v[204:211], v[178:181], v191, v191 op_sel_hi:[0,0,0]
	v_mfma_scale_f32_16x16x128_f8f6f4 v[170:173], v[10:17], v[204:211], v[170:173], v191, v191 op_sel_hi:[0,0,0]
	v_mfma_scale_f32_16x16x128_f8f6f4 v[162:165], v[2:9], v[214:221], v[162:165], v191, v191 op_sel_hi:[0,0,0]
	v_mfma_scale_f32_16x16x128_f8f6f4 v[154:157], v[10:17], v[214:221], v[154:157], v191, v191 op_sel_hi:[0,0,0]
	v_mfma_scale_f32_16x16x128_f8f6f4 v[146:149], v[2:9], v[222:229], v[146:149], v191, v191 op_sel_hi:[0,0,0]
	v_mfma_scale_f32_16x16x128_f8f6f4 v[138:141], v[10:17], v[222:229], v[138:141], v191, v191 op_sel_hi:[0,0,0]
	v_mfma_scale_f32_16x16x128_f8f6f4 v[130:133], v[2:9], v[230:237], v[130:133], v191, v191 op_sel_hi:[0,0,0]
	v_mfma_scale_f32_16x16x128_f8f6f4 v[122:125], v[10:17], v[230:237], v[122:125], v191, v191 op_sel_hi:[0,0,0]
	s_setprio 0
	s_setprio 1
	s_nop 1
	v_mfma_scale_f32_16x16x128_f8f6f4 v[182:185], v[18:25], v[204:211], v[182:185], v191, v191 op_sel_hi:[0,0,0]
	v_mfma_scale_f32_16x16x128_f8f6f4 v[174:177], v[26:33], v[204:211], v[174:177], v191, v191 op_sel_hi:[0,0,0]
	v_mfma_scale_f32_16x16x128_f8f6f4 v[166:169], v[18:25], v[214:221], v[166:169], v191, v191 op_sel_hi:[0,0,0]
	v_mfma_scale_f32_16x16x128_f8f6f4 v[158:161], v[26:33], v[214:221], v[158:161], v191, v191 op_sel_hi:[0,0,0]
	v_mfma_scale_f32_16x16x128_f8f6f4 v[150:153], v[18:25], v[222:229], v[150:153], v191, v191 op_sel_hi:[0,0,0]
	v_mfma_scale_f32_16x16x128_f8f6f4 v[142:145], v[26:33], v[222:229], v[142:145], v191, v191 op_sel_hi:[0,0,0]
	v_mfma_scale_f32_16x16x128_f8f6f4 v[134:137], v[18:25], v[230:237], v[134:137], v191, v191 op_sel_hi:[0,0,0]
	v_mfma_scale_f32_16x16x128_f8f6f4 v[126:129], v[26:33], v[230:237], v[126:129], v191, v191 op_sel_hi:[0,0,0]
	s_setprio 0
	s_barrier
	v_mov_b32_e32 v45, v1
	s_mov_b32 m0, s40
	ds_read_b128 v[204:207], v200 offset:49152
	ds_read_b128 v[208:211], v200 offset:50176
	ds_read_b128 v[214:217], v200 offset:51200
	ds_read_b128 v[218:221], v200 offset:52224
	ds_read_b128 v[222:225], v200 offset:53248
	ds_read_b128 v[226:229], v200 offset:54272
	ds_read_b128 v[230:233], v200 offset:55296
	ds_read_b128 v[234:237], v200 offset:56320
	s_nop 0
	global_load_lds_dwordx4 v45, s[34:35]
	v_mov_b32_e32 v45, v190
	s_mov_b32 m0, s41
	s_nop 0
	global_load_lds_dwordx4 v45, s[34:35]
	s_add_u32 s34, s34, 0x40000
	v_mov_b32_e32 v45, v1
	s_addc_u32 s35, s35, 0
	s_mov_b32 m0, s42
	s_nop 0
	global_load_lds_dwordx4 v45, s[34:35]
	v_mov_b32_e32 v45, v190
	s_mov_b32 m0, s43
	s_nop 0
	global_load_lds_dwordx4 v45, s[34:35]
	v_mov_b32_e32 v45, v192
	s_mov_b32 m0, s70
	s_nop 0
	global_load_lds_dwordx4 v45, s[30:31]
	v_mov_b32_e32 v45, v194
	s_mov_b32 m0, s71
	s_nop 0
	global_load_lds_dwordx4 v45, s[30:31]
	s_waitcnt vmcnt(8)
	s_waitcnt lgkmcnt(0)
	s_barrier
	s_setprio 1
	s_waitcnt lgkmcnt(0)
	s_nop 1
	v_mfma_scale_f32_16x16x128_f8f6f4 v[118:121], v[2:9], v[204:211], v[118:121], v191, v191 op_sel_hi:[0,0,0]
	v_mfma_scale_f32_16x16x128_f8f6f4 v[110:113], v[10:17], v[204:211], v[110:113], v191, v191 op_sel_hi:[0,0,0]
	v_mfma_scale_f32_16x16x128_f8f6f4 v[98:101], v[2:9], v[214:221], v[98:101], v191, v191 op_sel_hi:[0,0,0]
	v_mfma_scale_f32_16x16x128_f8f6f4 v[90:93], v[10:17], v[214:221], v[90:93], v191, v191 op_sel_hi:[0,0,0]
	v_mfma_scale_f32_16x16x128_f8f6f4 v[82:85], v[2:9], v[222:229], v[82:85], v191, v191 op_sel_hi:[0,0,0]
	v_mfma_scale_f32_16x16x128_f8f6f4 v[66:69], v[10:17], v[222:229], v[66:69], v191, v191 op_sel_hi:[0,0,0]
	v_mfma_scale_f32_16x16x128_f8f6f4 v[58:61], v[2:9], v[230:237], v[58:61], v191, v191 op_sel_hi:[0,0,0]
	v_mfma_scale_f32_16x16x128_f8f6f4 v[50:53], v[10:17], v[230:237], v[50:53], v191, v191 op_sel_hi:[0,0,0]
	s_setprio 0
	s_setprio 1
	s_nop 1
	v_mfma_scale_f32_16x16x128_f8f6f4 v[106:109], v[18:25], v[204:211], v[106:109], v191, v191 op_sel_hi:[0,0,0]
	v_mfma_scale_f32_16x16x128_f8f6f4 v[114:117], v[26:33], v[204:211], v[114:117], v191, v191 op_sel_hi:[0,0,0]
	v_mfma_scale_f32_16x16x128_f8f6f4 v[102:105], v[18:25], v[214:221], v[102:105], v191, v191 op_sel_hi:[0,0,0]
	v_mfma_scale_f32_16x16x128_f8f6f4 v[94:97], v[26:33], v[214:221], v[94:97], v191, v191 op_sel_hi:[0,0,0]
	v_mfma_scale_f32_16x16x128_f8f6f4 v[86:89], v[18:25], v[222:229], v[86:89], v191, v191 op_sel_hi:[0,0,0]
	v_mfma_scale_f32_16x16x128_f8f6f4 v[70:73], v[26:33], v[222:229], v[70:73], v191, v191 op_sel_hi:[0,0,0]
	v_mfma_scale_f32_16x16x128_f8f6f4 v[62:65], v[18:25], v[230:237], v[62:65], v191, v191 op_sel_hi:[0,0,0]
	v_mfma_scale_f32_16x16x128_f8f6f4 v[54:57], v[26:33], v[230:237], v[54:57], v191, v191 op_sel_hi:[0,0,0]
	s_setprio 0
	s_barrier
	s_add_i32 s52, s52, 2
	s_cmp_gt_u32 s52, 13
	s_cbranch_scc1 .LBB0_737

; __device__ __forceinline__ bool tile_order(long L, int nM, int nN, int& pm, int& pn) {
;     const int nwg = nM * nN; if (L >= nwg) return false;
;     int wgid = (int)L; { const int q = nwg / 8, r = nwg % 8, xcd = wgid % 8, off = wgid / 8; wgid = (xcd < r ? xcd * (q + 1) : r * (q + 1) + (xcd - r) * q) + off; }
;     const int nig = WGM * nN, gid = wgid / nig, fm = gid * WGM, gsz = (nM - fm) < WGM ? (nM - fm) : WGM;
;     pm = fm + ((wgid % nig) % gsz); pn = (wgid % nig) / gsz; return true;
;     __device__ __forceinline__ bool next(int i, Unit& u) const {
;         const int nM = __builtin_amdgcn_readfirstlane(tstart[NE]); int pm, pn; if (!tile_order((long)i * G + c, nM, nN, pm, pn)) return false;
;         int e = 0;
;         for (int j = 1; j < NE; ++j) e += (tstart[j] <= pm) ? 1 : 0;
;         e = __builtin_amdgcn_readfirstlane(e);
;         const int mt = __builtin_amdgcn_readfirstlane(pm - tstart[e]);
;         u.pm = pm; u.pn = pn; u.e = e;
;         u.avalid = __builtin_amdgcn_readfirstlane(cnt[e]) - mt * 256;
;         u.aidx = stok + (size_t)e * T + mt * 256;
;         u.aBase = GATHER ? A : A + (size_t)(GATHER_ ? (pm & 127) : pm) * 256 * ROWB;
;         u.bBase = Bt + ((size_t)e * nrowsB + (size_t)pn * 256) * ROWB;
.LBB0_804:
	v_mbcnt_lo_u32_b32 v7, -1, 0
	v_mbcnt_hi_u32_b32 v7, -1, v7
	v_lshlrev_b32_e32 v7, 2, v7
	v_add_u32_e32 v5, 0x27d00, v7
	ds_read_b32 v5, v5
	s_add_i32 s73, s73, 1
	s_mul_i32 s0, s73, s76
	s_mul_hi_u32 s1, s73, s33
	s_add_i32 s1, s1, s0
	s_mul_i32 s0, s73, s33
	s_waitcnt lgkmcnt(0)
	v_readlane_b32 s13, v5, 32
	s_add_u32 s30, s0, s38
	s_addc_u32 s31, s1, s48
	s_lshl_b32 s0, s13, 3
	s_ashr_i32 s1, s0, 31
	v_mov_b64_e32 v[2:3], s[0:1]
	v_cmp_ge_i64_e32 vcc, s[30:31], v[2:3]
	v_cmp_lt_i64_e64 s[0:1], s[30:31], v[2:3]
	s_cbranch_vccnz .LBB0_806
	s_ashr_i32 s12, s30, 31
	s_lshr_b32 s12, s12, 29
	s_add_i32 s12, s30, s12
	s_ashr_i32 s14, s12, 3
	s_and_b32 s12, s12, -8
	s_sub_i32 s12, s30, s12
	s_lshr_b32 s15, s12, 31
	s_add_i32 s15, s13, s15
	s_mul_i32 s12, s12, s15
	s_add_i32 s12, s12, s14
	s_ashr_i32 s14, s12, 31
	s_lshr_b32 s14, s14, 27
	s_add_i32 s14, s12, s14
	s_ashr_i32 s15, s14, 5
	s_lshl_b32 s15, s15, 2
	s_sub_i32 s13, s13, s15
	s_min_i32 s13, s13, 4
	s_abs_i32 s16, s13
	v_cvt_f32_u32_e32 v2, s16
	s_sub_i32 s18, 0, s16
	s_andn2_b32 s14, s14, 31
	s_sub_i32 s14, s12, s14
	v_rcp_iflag_f32_e32 v2, v2
	s_abs_i32 s12, s14
	s_xor_b32 s17, s14, s13
	s_ashr_i32 s17, s17, 31
	v_mul_f32_e32 v2, 0x4f7ffffe, v2
	v_cvt_u32_f32_e32 v2, v2
	s_nop 0
	v_readfirstlane_b32 s19, v2
	s_mul_i32 s18, s18, s19
	s_mul_hi_u32 s18, s19, s18
	s_add_i32 s19, s19, s18
	s_mul_hi_u32 s18, s12, s19
	s_mul_i32 s19, s18, s16
	s_sub_i32 s12, s12, s19
	s_add_i32 s20, s18, 1
	s_sub_i32 s19, s12, s16
	s_cmp_ge_u32 s12, s16
	s_cselect_b32 s18, s20, s18
	s_cselect_b32 s12, s19, s12
	s_add_i32 s19, s18, 1
	s_cmp_ge_u32 s12, s16
	s_cselect_b32 s12, s19, s18
	s_xor_b32 s12, s12, s17
	s_sub_i32 s12, s12, s17
	s_mul_i32 s13, s12, s13
	s_sub_i32 s13, s14, s13
	s_add_i32 s14, s15, s13
	v_cmp_ge_i32_e32 vcc, s14, v5
	s_ashr_i32 s15, s14, 31
	s_lshl_b64 s[18:19], s[14:15], 19
	s_nop 3
	s_and_b32 vcc_lo, vcc_lo, 0xfffffffe
	s_bcnt1_i32_b32 s96, vcc_lo
	s_ashr_i32 s97, s96, 31
	s_add_u32 s92, s43, s18
	s_addc_u32 s93, s44, s19
	s_ashr_i32 s13, s12, 31
	s_lshl_b64 s[20:21], s[12:13], 19
	s_lshl_b64 s[30:31], s[96:97], 22
	s_add_u32 s13, s45, s20
	s_addc_u32 s15, s46, s21
	s_add_u32 s94, s13, s30
	s_addc_u32 s95, s15, s31
